# v65 + in-proj tile order: gelu-stat tiles (2,3) swapped with sigmoid tiles (12,13): statistics tiles on the five-unit workgroups in round 3
# baseline (speedup 1.0000x reference)
;     __device__ bool next(int i, Unit& u) const { if (!base.next(i >> 1, u)) return false; if (i & 1) { u.pm += MTOK / BM; u.pn += DM / BM; } return true; }
;   __device__ __forceinline__ bool next(int i,AttnUnit&u)const{ if(i>=2||vcu>=256)return false; const int s=vcu&3; u.bh=vcu>>2; u.qb=(i==0)?7-s:s; return true; }
;     __host__ __device__ bool next(int i, Unit& u) const {
;         const int L = i * G + c; if (L >= nwg) return false;
;         int wgid = L; { const int q = nwg / NXCD, r = nwg % NXCD, xcd = wgid % NXCD, off = wgid / NXCD; wgid = (xcd < r ? xcd * (q + 1) : r * (q + 1) + (xcd - r) * q) + off; }
;         const int nig = WGM * nN, gid = wgid / nig, fm = gid * WGM, gsz = (nM - fm) < WGM ? (nM - fm) : WGM;
;         u.pm = fm + ((wgid % nig) % gsz); u.pn = (wgid % nig) / gsz; u.half = 0; return true;
.LBB0_382:
	s_ashr_i32 s4, s21, 31
	s_lshr_b32 s4, s4, 29
	s_add_i32 s4, s21, s4
	s_ashr_i32 s5, s4, 3
	s_and_b32 s4, s4, -8
	s_sub_i32 s4, s21, s4
	s_cmp_lt_i32 s4, 0
	s_movk_i32 s6, 0x91
	s_cselect_b32 s6, s6, 0x90
	s_mul_i32 s4, s4, s6
	s_add_i32 s4, s4, s5
	s_mul_hi_i32 s5, s4, 0x38e38e39
	s_lshr_b32 s6, s5, 31
	s_ashr_i32 s5, s5, 5
	s_add_i32 s5, s5, s6
	s_lshl_b32 s6, s5, 3
	s_mulk_i32 s5, 0x90
	s_sub_i32 s4, s4, s5
	s_bfe_u32 s5, s4, 0x3001c
	s_add_i32 s5, s4, s5
	s_sext_i32_i16 s7, s5
	s_and_b32 s5, s5, 0xfff8
	s_sub_i32 s4, s4, s5
	s_sext_i32_i16 s4, s4
	s_add_i32 s18, s6, s4
	s_ashr_i32 s70, s7, 3
	s_mul_i32 s4, s70, 5
	s_cmp_lt_u32 s70, 12
	s_cbranch_scc0 .Lpn_hi0
	s_mov_b32 s6, 0x8a46b020
	s_mov_b32 s7, 0x5a92839
	s_branch .Lpn_go0
.Lpn_hi0:
	s_sub_i32 s4, s4, 60
	s_mov_b32 s6, 0x2307b862
	s_mov_b32 s7, 0

;     __device__ bool next(int i, Unit& u) const { if (!base.next(i >> 1, u)) return false; if (i & 1) { u.pm += MTOK / BM; u.pn += DM / BM; } return true; }
;   __device__ __forceinline__ bool next(int i,AttnUnit&u)const{ if(i>=2||vcu>=256)return false; const int s=vcu&3; u.bh=vcu>>2; u.qb=(i==0)?7-s:s; return true; }
;     __host__ __device__ bool next(int i, Unit& u) const {
;         const int L = i * G + c; if (L >= nwg) return false;
;         int wgid = L; { const int q = nwg / NXCD, r = nwg % NXCD, xcd = wgid % NXCD, off = wgid / NXCD; wgid = (xcd < r ? xcd * (q + 1) : r * (q + 1) + (xcd - r) * q) + off; }
;         const int nig = WGM * nN, gid = wgid / nig, fm = gid * WGM, gsz = (nM - fm) < WGM ? (nM - fm) : WGM;
;         u.pm = fm + ((wgid % nig) % gsz); u.pn = (wgid % nig) / gsz; u.half = 0; return true;
; template <class Epi, class Sched, bool ALIGN_EPI = false, bool SP2 = false>
; __device__ __forceinline__ void gemm_phase(PG8_LAS unsigned char* lds, const Gemm g, const Sched& S, const Epi& E) {
;     ...
;         const bool has_next = S.next(ui + 1, nxt);
;         const char* nA = has_next ? (const char*)g.A + (size_t)nxt.pm * tstep + (nxt.half == 2 ? hstep : (size_t)0) : cA; const char* nB = has_next ? (const char*)g.Bt + (size_t)nxt.pn * tstep : cB;
.LBB0_392:
	s_add_i32 s72, s72, 1
	s_mul_i32 s10, s72, s33
	s_add_i32 s10, s10, s21
	s_cmpk_lt_i32 s10, 0x480
	s_cselect_b64 s[64:65], -1, 0
	s_cmpk_gt_i32 s10, 0x47f
	s_cbranch_scc1 .LBB0_394
	s_ashr_i32 s11, s10, 31
	s_lshr_b32 s11, s11, 29
	s_add_i32 s11, s10, s11
	s_ashr_i32 s12, s11, 3
	s_and_b32 s11, s11, -8
	s_sub_i32 s10, s10, s11
	s_cmp_lt_i32 s10, 0
	s_movk_i32 s11, 0x91
	s_cselect_b32 s11, s11, 0x90
	s_mul_i32 s10, s10, s11
	s_add_i32 s10, s10, s12
	s_mul_hi_i32 s11, s10, 0x38e38e39
	s_lshr_b32 s12, s11, 31
	s_ashr_i32 s11, s11, 5
	s_add_i32 s11, s11, s12
	s_lshl_b32 s12, s11, 3
	s_mulk_i32 s11, 0x90
	s_sub_i32 s10, s10, s11
	s_bfe_u32 s11, s10, 0x3001c
	s_add_i32 s11, s10, s11
	s_sext_i32_i16 s13, s11
	s_and_b32 s11, s11, 0xfff8
	s_sub_i32 s10, s10, s11
	s_sext_i32_i16 s10, s10
	s_add_i32 s60, s12, s10
	s_ashr_i32 s62, s13, 3
	s_mul_i32 s10, s62, 5
	s_cmp_lt_u32 s62, 12
	s_cbranch_scc0 .Lpn_hi1
	s_mov_b32 s12, 0x8a46b020
	s_mov_b32 s13, 0x5a92839
	s_branch .Lpn_go1
.Lpn_hi1:
	s_sub_i32 s10, s10, 60
	s_mov_b32 s12, 0x2307b862
	s_mov_b32 s13, 0
